# moe_gu: per-thread staging row/column offsets cached once per phase in the free v225; a_request (unit head) 57->21 instrs and a_finish (last K trip) 78->22 instrs (on top of v55)
# speedup vs baseline: 1.0074x; 1.0003x over previous
.LBB0_1539:
	v_mov_b32_e32 v161, v173
	v_lshl_add_u64 v[2:3], s[24:25], 0, v[160:161]
	v_mov_b32_e32 v163, v173
	s_add_i32 s71, s44, 0x18000
	v_lshl_add_u64 v[4:5], s[24:25], 0, v[162:163]
	v_lshl_add_u64 v[2:3], v[2:3], 0, s[40:41]
	s_mov_b32 m0, s71
	s_add_i32 s80, s44, 0x1a000
	v_readlane_b32 s2, v253, 60
	v_mov_b32_e32 v167, v173
	s_waitcnt vmcnt(4)
	s_barrier
	global_load_lds_dwordx4 v[2:3], off
	v_lshl_add_u64 v[2:3], v[4:5], 0, s[40:41]
	s_mov_b32 m0, s80
	v_readlane_b32 s3, v253, 61
	s_add_i32 s81, s44, 0x8000
	s_lshl_b32 s11, s12, 6
	v_mov_b32_e32 v171, v173
	global_load_lds_dwordx4 v[2:3], off
	v_lshl_add_u64 v[2:3], s[2:3], 0, v[166:167]
	s_mov_b32 m0, s81
	s_add_i32 s82, s44, 0xa000
	global_load_lds_dwordx4 v[2:3], off
	v_lshl_add_u64 v[2:3], s[2:3], 0, v[170:171]
	s_add_u32 s2, s24, 0x20080
	s_mov_b32 m0, s82
	s_addc_u32 s3, s25, 0
	s_add_i32 s83, s44, 0x1c000
	global_load_lds_dwordx4 v[2:3], off
	v_lshl_add_u64 v[2:3], s[2:3], 0, v[160:161]
	s_mov_b32 m0, s83
	s_add_i32 s85, s44, 0x1e000
	global_load_lds_dwordx4 v[2:3], off
	v_lshl_add_u64 v[2:3], s[2:3], 0, v[162:163]
	s_mov_b32 m0, s85
	v_and_b32_e32 v1, 0xc0, v1
	global_load_lds_dwordx4 v[2:3], off
	v_bfe_u32 v2, v188, 4, 2
	v_lshlrev_b32_e32 v3, 4, v2
	v_and_b32_e32 v4, 12, v188
	v_or3_b32 v167, v3, v1, v4
	v_lshrrev_b32_e32 v3, 2, v0
	v_lshlrev_b32_e32 v0, 3, v0
	s_waitcnt vmcnt(6)
	v_and_or_b32 v194, v0, 24, s1
	s_lshl_b32 s1, s1, 2
	s_movk_i32 s0, 0x80
	s_lshr_b32 s2, s14, 2
	s_add_i32 s3, 0, 0x20800
	v_lshlrev_b32_e32 v1, 2, v2
	v_lshl_or_b32 v0, v2, 5, s1
	v_readlane_b32 s22, v253, 44
	v_cmp_gt_i32_e64 s[6:7], s0, v188
	s_add_i32 s87, s3, s2
	v_or3_b32 v171, v1, v3, s11
	v_add_u32_e32 v195, s3, v0
	s_mov_b32 s57, 0
	v_mov_b32_e32 v219, s13
	v_mov_b32_e32 v220, s10
	v_readlane_b32 s23, v253, 45
	s_barrier
	v_lshrrev_b32_e32 v0, 6, v188
	v_and_b32_e32 v1, 63, v188
	v_lshlrev_b32_e32 v1, 4, v1
	v_lshrrev_b32_e32 v2, 4, v1
	v_and_b32_e32 v2, 32, v2
	v_xor_b32_e32 v1, v1, v2
	v_lshrrev_b32_e32 v2, 1, v0
	v_lshlrev_b32_e32 v2, 4, v2
	v_lshrrev_b32_e32 v3, 6, v1
	v_add_u32_e32 v2, v2, v3
	v_and_b32_e32 v0, 1, v0
	v_lshlrev_b32_e32 v0, 6, v0
	v_and_b32_e32 v1, 63, v1
	v_add_u32_e32 v0, v0, v1
	v_lshl_or_b32 v225, v0, 16, v2
	s_branch .LBB0_1541

.LBB0_1551:
	v_mov_b32_e32 v32, 0
	s_andn2_b64 vcc, exec, s[2:3]
	v_mov_b32_e32 v2, v174
	v_mov_b32_e32 v3, v168
	v_mov_b32_e32 v4, v170
	v_mov_b32_e32 v1, v166
	s_mov_b64 s[16:17], s[24:25]
	s_mov_b64 s[18:19], s[22:23]
	v_mov_b32_e32 v165, 0
	v_mov_b32_e32 v223, 0
	v_mov_b32_e32 v221, 0
	v_mov_b32_e32 v224, 0
	s_cbranch_vccnz .LBB0_1553
	v_add_u32_e32 v4, -1, v0
	v_and_b32_e32 v1, 0xff, v225
	v_min_i32_e32 v2, v1, v4
	v_ashrrev_i32_e32 v3, 31, v2
	v_lshl_add_u64 v[2:3], v[2:3], 2, s[12:13]
	v_add_u32_e32 v5, 0x80, v1
	global_load_dword v165, v[2:3], off
	v_min_i32_e32 v2, v5, v4
	v_ashrrev_i32_e32 v3, 31, v2
	v_lshl_add_u64 v[2:3], v[2:3], 2, s[12:13]
	v_add_u32_e32 v5, 64, v1
	global_load_dword v221, v[2:3], off
	v_min_i32_e32 v2, v5, v4
	v_ashrrev_i32_e32 v3, 31, v2
	v_lshl_add_u64 v[2:3], v[2:3], 2, s[12:13]
	v_add_u32_e32 v5, 0xc0, v1
	global_load_dword v223, v[2:3], off
	v_min_i32_e32 v2, v5, v4
	v_ashrrev_i32_e32 v3, 31, v2
	v_lshl_add_u64 v[2:3], v[2:3], 2, s[12:13]
	global_load_dword v224, v[2:3], off
	v_readlane_b32 s18, v253, 44
	v_mov_b32_e32 v222, v0
	v_mov_b32_e32 v2, v218
	v_mov_b32_e32 v3, v216
	v_mov_b32_e32 v4, v217
	v_mov_b32_e32 v1, v215
	s_mov_b64 s[16:17], s[10:11]
	v_readlane_b32 s19, v253, 45

.LBB0_1556:
	s_cmp_eq_u32 s64, 4
	s_cselect_b64 s[24:25], -1, 0
	s_cmp_lg_u32 s64, 4
	s_cbranch_scc1 .LBB0_1554
	s_andn2_b64 vcc, exec, s[20:21]
	s_cbranch_vccnz .LBB0_1559
	v_and_b32_e32 v3, 0xff, v225
	v_lshrrev_b32_e32 v0, 16, v225
	v_cmp_lt_i32_e32 vcc, v3, v222
	v_lshlrev_b32_e32 v2, 10, v165
	v_add_u32_e32 v1, 0x80, v3
	v_cndmask_b32_e32 v2, 0, v2, vcc
	v_add_u32_e32 v215, v0, v2
	v_cmp_lt_i32_e32 vcc, v1, v222
	v_lshlrev_b32_e32 v2, 10, v221
	v_add_u32_e32 v1, 64, v3
	v_cndmask_b32_e32 v2, 0, v2, vcc
	v_add_u32_e32 v216, v0, v2
	v_cmp_lt_i32_e32 vcc, v1, v222
	v_lshlrev_b32_e32 v2, 10, v223
	v_add_u32_e32 v1, 0xc0, v3
	v_cndmask_b32_e32 v2, 0, v2, vcc
	v_add_u32_e32 v217, v0, v2
	v_cmp_lt_i32_e32 vcc, v1, v222
	v_lshlrev_b32_e32 v2, 10, v224
	s_nop 0
	v_cndmask_b32_e32 v2, 0, v2, vcc
	v_add_u32_e32 v218, v0, v2
